# v74 plus every workgroup starts the XCD L2 writeback (buffer_wbl2 sc1, not waited) when it arrives at a grid barrier, so the last arriver's release writeback finds little left
# baseline (speedup 1.0000x reference)
.LBB0_269:
	v_readlane_b32 s2, v252, 1
	v_readlane_b32 s3, v252, 2
	v_mov_b32_e32 v0, 1
	v_sub_u32_e32 v5, 0, v3
	s_nop 2
	buffer_wbl2 sc1
	global_atomic_add v4, v1, v0, s[2:3] sc0
	v_cvt_f32_u32_e32 v0, v3
	v_rcp_iflag_f32_e32 v0, v0
	s_nop 0
	v_mul_f32_e32 v0, 0x4f7ffffe, v0
	v_cvt_u32_f32_e32 v0, v0
	v_mul_lo_u32 v5, v5, v0
	v_mul_hi_u32 v5, v0, v5
	v_add_u32_e32 v0, v0, v5
	s_waitcnt vmcnt(0)
	v_mul_hi_u32 v0, v4, v0
	v_mul_lo_u32 v5, v0, v3
	v_sub_u32_e32 v5, v4, v5
	v_add_u32_e32 v6, 1, v0
	v_cmp_ge_u32_e32 vcc, v5, v3
	v_add_u32_e32 v4, 1, v4
	s_nop 0
	v_cndmask_b32_e32 v0, v0, v6, vcc
	v_sub_u32_e32 v6, v5, v3
	v_cndmask_b32_e32 v5, v5, v6, vcc
	v_add_u32_e32 v6, 1, v0
	v_cmp_ge_u32_e32 vcc, v5, v3
	s_nop 1
	v_cndmask_b32_e32 v0, v0, v6, vcc
	v_mul_lo_u32 v5, v3, v0
	v_add_u32_e32 v3, v5, v3
	v_cmp_ne_u32_e32 vcc, v4, v3
	s_and_saveexec_b64 s[2:3], vcc
	s_xor_b64 s[2:3], exec, s[2:3]
	s_cbranch_execz .LBB0_283
	v_readlane_b32 s4, v252, 3
	v_readlane_b32 s5, v252, 4
	s_waitcnt lgkmcnt(0)
	s_nop 3
	global_load_dword v2, v1, s[4:5] sc1
	s_waitcnt vmcnt(0)
	v_cmp_eq_u32_e32 vcc, v2, v0
	s_and_saveexec_b64 s[4:5], vcc
	s_cbranch_execz .LBB0_282
	s_mov_b32 s17, 1
	s_mov_b64 s[6:7], 0
	s_branch .LBB0_273

.LBB0_438:
	v_readlane_b32 s2, v252, 1
	v_readlane_b32 s3, v252, 2
	v_mov_b32_e32 v0, 1
	v_sub_u32_e32 v5, 0, v3
	s_nop 2
	buffer_wbl2 sc1
	global_atomic_add v4, v1, v0, s[2:3] sc0
	v_cvt_f32_u32_e32 v0, v3
	v_rcp_iflag_f32_e32 v0, v0
	s_nop 0
	v_mul_f32_e32 v0, 0x4f7ffffe, v0
	v_cvt_u32_f32_e32 v0, v0
	v_mul_lo_u32 v5, v5, v0
	v_mul_hi_u32 v5, v0, v5
	v_add_u32_e32 v0, v0, v5
	s_waitcnt vmcnt(0)
	v_mul_hi_u32 v0, v4, v0
	v_mul_lo_u32 v5, v0, v3
	v_sub_u32_e32 v5, v4, v5
	v_add_u32_e32 v6, 1, v0
	v_cmp_ge_u32_e32 vcc, v5, v3
	v_add_u32_e32 v4, 1, v4
	s_nop 0
	v_cndmask_b32_e32 v0, v0, v6, vcc
	v_sub_u32_e32 v6, v5, v3
	v_cndmask_b32_e32 v5, v5, v6, vcc
	v_add_u32_e32 v6, 1, v0
	v_cmp_ge_u32_e32 vcc, v5, v3
	s_nop 1
	v_cndmask_b32_e32 v0, v0, v6, vcc
	v_mul_lo_u32 v5, v3, v0
	v_add_u32_e32 v3, v5, v3
	v_cmp_ne_u32_e32 vcc, v4, v3
	s_and_saveexec_b64 s[2:3], vcc
	s_xor_b64 s[2:3], exec, s[2:3]
	s_cbranch_execz .LBB0_452
	v_readlane_b32 s4, v252, 3
	v_readlane_b32 s5, v252, 4
	s_waitcnt lgkmcnt(0)
	s_nop 3
	global_load_dword v2, v1, s[4:5] sc1
	s_waitcnt vmcnt(0)
	v_cmp_eq_u32_e32 vcc, v2, v0
	s_and_saveexec_b64 s[4:5], vcc
	s_cbranch_execz .LBB0_451
	s_mov_b32 s21, 1
	s_mov_b64 s[6:7], 0
	s_branch .LBB0_442

.LBB0_1471:
	v_readlane_b32 s2, v252, 1
	v_readlane_b32 s3, v252, 2
	v_mov_b32_e32 v0, 1
	v_sub_u32_e32 v5, 0, v3
	s_nop 2
	buffer_wbl2 sc1
	global_atomic_add v4, v1, v0, s[2:3] sc0
	v_cvt_f32_u32_e32 v0, v3
	v_rcp_iflag_f32_e32 v0, v0
	s_nop 0
	v_mul_f32_e32 v0, 0x4f7ffffe, v0
	v_cvt_u32_f32_e32 v0, v0
	v_mul_lo_u32 v5, v5, v0
	v_mul_hi_u32 v5, v0, v5
	v_add_u32_e32 v0, v0, v5
	s_waitcnt vmcnt(0)
	v_mul_hi_u32 v0, v4, v0
	v_mul_lo_u32 v5, v0, v3
	v_sub_u32_e32 v5, v4, v5
	v_add_u32_e32 v6, 1, v0
	v_cmp_ge_u32_e32 vcc, v5, v3
	v_add_u32_e32 v4, 1, v4
	s_nop 0
	v_cndmask_b32_e32 v0, v0, v6, vcc
	v_sub_u32_e32 v6, v5, v3
	v_cndmask_b32_e32 v5, v5, v6, vcc
	v_add_u32_e32 v6, 1, v0
	v_cmp_ge_u32_e32 vcc, v5, v3
	s_nop 1
	v_cndmask_b32_e32 v0, v0, v6, vcc
	v_mul_lo_u32 v5, v3, v0
	v_add_u32_e32 v3, v5, v3
	v_cmp_ne_u32_e32 vcc, v4, v3
	s_and_saveexec_b64 s[2:3], vcc
	s_xor_b64 s[2:3], exec, s[2:3]
	s_cbranch_execz .LBB0_1485
	v_readlane_b32 s4, v252, 3
	v_readlane_b32 s5, v252, 4
	s_waitcnt lgkmcnt(0)
	s_nop 3
	global_load_dword v2, v1, s[4:5] sc1
	s_waitcnt vmcnt(0)
	v_cmp_eq_u32_e32 vcc, v2, v0
	s_and_saveexec_b64 s[4:5], vcc
	s_cbranch_execz .LBB0_1484
	s_mov_b32 s16, 1
	s_mov_b64 s[6:7], 0
	s_branch .LBB0_1475
